# gate-tile gather of the w_in conversion batched (60 loads in flight) in P0 and mixer phase; FF1 epilogue stat loads hoisted
# speedup vs baseline: 1.0058x; 1.0058x over previous
.LBB0_129:
	s_cmp_eq_u32 s26, -2
	v_mov_b64_e32 v[4:5], s[18:19]
	s_cselect_b64 s[6:7], -1, 0
	v_mad_i64_i32 v[4:5], s[20:21], v86, s80, v[4:5]
	s_and_b64 s[20:21], s[6:7], s[4:5]
	v_mov_b32_e32 v9, 0
	v_mov_b32_e32 v8, 0
	s_waitcnt vmcnt(0)
	v_mov_b32_e32 v8, 0
	v_mov_b32_e32 v9, 0
	v_mov_b32_e32 v46, 0
	v_mov_b32_e32 v40, 0
	v_mov_b32_e32 v42, 0
	v_mov_b32_e32 v48, 0
	v_mov_b32_e32 v52, 0
	v_mov_b32_e32 v45, 0
	v_mov_b32_e32 v51, 0
	v_mov_b32_e32 v54, 0
	v_mov_b32_e32 v60, 0
	v_mov_b32_e32 v50, 0
	v_mov_b32_e32 v56, 0
	v_mov_b32_e32 v62, 0
	v_mov_b32_e32 v88, 0
	v_mov_b32_e32 v59, 0
	v_mov_b32_e32 v75, 0
	v_mov_b32_e32 v90, 0
	v_mov_b32_e32 v96, 0
	v_mov_b32_e32 v73, 0
	v_mov_b32_e32 v92, 0
	v_mov_b32_e32 v98, 0
	v_mov_b32_e32 v102, 0
	v_mov_b32_e32 v95, 0
	v_mov_b32_e32 v101, 0
	v_mov_b32_e32 v104, 0
	v_mov_b32_e32 v110, 0
	v_mov_b32_e32 v100, 0
	v_mov_b32_e32 v106, 0
	v_mov_b32_e32 v112, 0
	v_mov_b32_e32 v116, 0
	v_mov_b32_e32 v109, 0
	v_mov_b32_e32 v115, 0
	v_mov_b32_e32 v118, 0
	v_mov_b32_e32 v124, 0
	v_mov_b32_e32 v114, 0
	v_mov_b32_e32 v120, 0
	v_mov_b32_e32 v126, 0
	v_mov_b32_e32 v130, 0
	v_mov_b32_e32 v123, 0
	v_mov_b32_e32 v129, 0
	v_mov_b32_e32 v132, 0
	v_mov_b32_e32 v138, 0
	v_mov_b32_e32 v128, 0
	v_mov_b32_e32 v134, 0
	v_mov_b32_e32 v140, 0
	v_mov_b32_e32 v144, 0
	v_mov_b32_e32 v137, 0
	v_mov_b32_e32 v143, 0
	v_mov_b32_e32 v146, 0
	v_mov_b32_e32 v152, 0
	v_mov_b32_e32 v142, 0
	v_mov_b32_e32 v148, 0
	v_mov_b32_e32 v154, 0
	v_mov_b32_e32 v158, 0
	v_mov_b32_e32 v151, 0
	v_mov_b32_e32 v157, 0
	v_mov_b32_e32 v160, 0
	v_mov_b32_e32 v164, 0
	v_mov_b32_e32 v156, 0
	s_and_saveexec_b64 s[6:7], s[20:21]
	s_cbranch_execz .Lgate_batch_done_p0
	v_mov_b32_e32 v10, 0x4d180
	v_mov_b32_e32 v11, 0
	v_lshlrev_b32_e32 v64, 2, v70
	v_lshl_add_u64 v[4:5], v[4:5], 0, v[64:65]
	global_load_dword v8, v[4:5], off
	global_load_dword v9, v[4:5], off offset:4
	global_load_dword v46, v[4:5], off offset:8
	global_load_dword v40, v[4:5], off offset:12
	v_lshl_add_u64 v[4:5], v[4:5], 0, v[10:11]
	global_load_dword v42, v[4:5], off
	global_load_dword v48, v[4:5], off offset:4
	global_load_dword v52, v[4:5], off offset:8
	global_load_dword v45, v[4:5], off offset:12
	v_lshl_add_u64 v[4:5], v[4:5], 0, v[10:11]
	global_load_dword v51, v[4:5], off
	global_load_dword v54, v[4:5], off offset:4
	global_load_dword v60, v[4:5], off offset:8
	global_load_dword v50, v[4:5], off offset:12
	v_lshl_add_u64 v[4:5], v[4:5], 0, v[10:11]
	global_load_dword v56, v[4:5], off
	global_load_dword v62, v[4:5], off offset:4
	global_load_dword v88, v[4:5], off offset:8
	global_load_dword v59, v[4:5], off offset:12
	v_lshl_add_u64 v[4:5], v[4:5], 0, v[10:11]
	global_load_dword v75, v[4:5], off
	global_load_dword v90, v[4:5], off offset:4
	global_load_dword v96, v[4:5], off offset:8
	global_load_dword v73, v[4:5], off offset:12
	v_lshl_add_u64 v[4:5], v[4:5], 0, v[10:11]
	global_load_dword v92, v[4:5], off
	global_load_dword v98, v[4:5], off offset:4
	global_load_dword v102, v[4:5], off offset:8
	global_load_dword v95, v[4:5], off offset:12
	v_lshl_add_u64 v[4:5], v[4:5], 0, v[10:11]
	global_load_dword v101, v[4:5], off
	global_load_dword v104, v[4:5], off offset:4
	global_load_dword v110, v[4:5], off offset:8
	global_load_dword v100, v[4:5], off offset:12
	v_lshl_add_u64 v[4:5], v[4:5], 0, v[10:11]
	global_load_dword v106, v[4:5], off
	global_load_dword v112, v[4:5], off offset:4
	global_load_dword v116, v[4:5], off offset:8
	global_load_dword v109, v[4:5], off offset:12
	v_lshl_add_u64 v[4:5], v[4:5], 0, v[10:11]
	global_load_dword v115, v[4:5], off
	global_load_dword v118, v[4:5], off offset:4
	global_load_dword v124, v[4:5], off offset:8
	global_load_dword v114, v[4:5], off offset:12
	v_lshl_add_u64 v[4:5], v[4:5], 0, v[10:11]
	global_load_dword v120, v[4:5], off
	global_load_dword v126, v[4:5], off offset:4
	global_load_dword v130, v[4:5], off offset:8
	global_load_dword v123, v[4:5], off offset:12
	v_lshl_add_u64 v[4:5], v[4:5], 0, v[10:11]
	global_load_dword v129, v[4:5], off
	global_load_dword v132, v[4:5], off offset:4
	global_load_dword v138, v[4:5], off offset:8
	global_load_dword v128, v[4:5], off offset:12
	v_lshl_add_u64 v[4:5], v[4:5], 0, v[10:11]
	global_load_dword v134, v[4:5], off
	global_load_dword v140, v[4:5], off offset:4
	global_load_dword v144, v[4:5], off offset:8
	global_load_dword v137, v[4:5], off offset:12
	v_lshl_add_u64 v[4:5], v[4:5], 0, v[10:11]
	global_load_dword v143, v[4:5], off
	global_load_dword v146, v[4:5], off offset:4
	global_load_dword v152, v[4:5], off offset:8
	global_load_dword v142, v[4:5], off offset:12
	v_lshl_add_u64 v[4:5], v[4:5], 0, v[10:11]
	global_load_dword v148, v[4:5], off
	global_load_dword v154, v[4:5], off offset:4
	global_load_dword v158, v[4:5], off offset:8
	global_load_dword v151, v[4:5], off offset:12
	v_lshl_add_u64 v[4:5], v[4:5], 0, v[10:11]
	global_load_dword v157, v[4:5], off
	global_load_dword v160, v[4:5], off offset:4
	global_load_dword v164, v[4:5], off offset:8
	global_load_dword v156, v[4:5], off offset:12
.Lgate_batch_done_p0:
	s_or_b64 exec, exec, s[6:7]
	s_waitcnt vmcnt(0)
	v_mul_f32_e32 v10, v7, v8
	v_cvt_pk_bf16_f32 v10, v10, v10
	s_nop 0
	v_lshlrev_b32_e32 v41, 16, v10
	ds_write_b32 v180, v41
	s_waitcnt vmcnt(0)
	v_mul_f32_e32 v10, v7, v9
	v_cvt_pk_bf16_f32 v10, v10, v10
	v_lshlrev_b32_e32 v43, 16, v10
	ds_write_b32 v180, v43 offset:4
	s_waitcnt vmcnt(0)
	v_mul_f32_e32 v10, v7, v46
	v_cvt_pk_bf16_f32 v10, v10, v10
	s_nop 0
	v_lshlrev_b32_e32 v47, 16, v10
	ds_write_b32 v180, v47 offset:8
	s_waitcnt vmcnt(0)
	v_mul_f32_e32 v4, v7, v40
	v_cvt_pk_bf16_f32 v4, v4, v4
	v_lshlrev_b32_e32 v7, 16, v4
	v_cndmask_b32_e64 v4, 0, 1, s[22:23]
	v_cmp_ne_u32_e64 s[6:7], 1, v4
	s_andn2_b64 vcc, exec, s[22:23]
	v_mov_b32_e32 v10, 0
	v_mov_b32_e32 v11, v85
	ds_write_b32 v180, v7 offset:12
	s_cbranch_vccnz .LBB0_139
	global_load_dword v5, v[0:1], off offset:16
	global_load_dword v4, v[2:3], off offset:16
	s_waitcnt vmcnt(0)
	v_pk_mul_f32 v[10:11], v[84:85], v[4:5] op_sel:[1,0]
.LBB0_139:
	v_or_b32_e32 v12, 4, v86
	v_mov_b64_e32 v[4:5], s[18:19]
	v_mad_i64_i32 v[4:5], s[22:23], v12, s80, v[4:5]
	s_waitcnt vmcnt(0)
	v_mul_f32_e32 v12, v11, v42
	v_cvt_pk_bf16_f32 v12, v12, v12
	v_lshlrev_b32_e32 v44, 16, v12
	ds_write_b32 v180, v44 offset:1040
	s_waitcnt vmcnt(0)
	v_mul_f32_e32 v12, v11, v48
	v_cvt_pk_bf16_f32 v12, v12, v12
	s_nop 0
	v_lshlrev_b32_e32 v49, 16, v12
	ds_write_b32 v180, v49 offset:1044
	s_waitcnt vmcnt(0)
	v_mul_f32_e32 v12, v11, v52
	v_cvt_pk_bf16_f32 v12, v12, v12
	v_lshlrev_b32_e32 v55, 16, v12
	v_mov_b32_e32 v12, 0
	ds_write_b32 v180, v55 offset:1048
	s_waitcnt vmcnt(0)
	v_mul_f32_e32 v4, v11, v45
	v_cvt_pk_bf16_f32 v4, v4, v4
	s_and_b64 vcc, exec, s[6:7]
	v_lshlrev_b32_e32 v11, 16, v4
	v_mov_b32_e32 v13, v85
	ds_write_b32 v180, v11 offset:1052
	s_cbranch_vccnz .LBB0_149
	global_load_dword v5, v[0:1], off offset:32
	global_load_dword v4, v[2:3], off offset:32
	s_waitcnt vmcnt(0)
	v_pk_mul_f32 v[12:13], v[84:85], v[4:5] op_sel:[1,0]
.LBB0_149:
	v_or_b32_e32 v14, 8, v86
	v_mov_b64_e32 v[4:5], s[18:19]
	v_mad_i64_i32 v[4:5], s[22:23], v14, s80, v[4:5]
	s_waitcnt vmcnt(0)
	v_mul_f32_e32 v14, v13, v51
	v_cvt_pk_bf16_f32 v14, v14, v14
	s_nop 0
	v_lshlrev_b32_e32 v53, 16, v14
	ds_write_b32 v180, v53 offset:2080
	s_waitcnt vmcnt(0)
	v_mul_f32_e32 v14, v13, v54
	v_cvt_pk_bf16_f32 v14, v14, v14
	v_lshlrev_b32_e32 v57, 16, v14
	ds_write_b32 v180, v57 offset:2084
	s_waitcnt vmcnt(0)
	v_mul_f32_e32 v14, v13, v60
	v_cvt_pk_bf16_f32 v14, v14, v14
	s_nop 0
	v_lshlrev_b32_e32 v61, 16, v14
	ds_write_b32 v180, v61 offset:2088
	s_waitcnt vmcnt(0)
	v_mul_f32_e32 v4, v13, v50
	v_cvt_pk_bf16_f32 v4, v4, v4
	v_lshlrev_b32_e32 v13, 16, v4
	s_and_b64 vcc, exec, s[6:7]
	v_mov_b32_e32 v14, 0
	v_mov_b32_e32 v15, v85
	ds_write_b32 v180, v13 offset:2092
	s_cbranch_vccnz .LBB0_159
	global_load_dword v5, v[0:1], off offset:48
	global_load_dword v4, v[2:3], off offset:48
	s_waitcnt vmcnt(0)
	v_pk_mul_f32 v[14:15], v[84:85], v[4:5] op_sel:[1,0]
.LBB0_159:
	v_or_b32_e32 v16, 12, v86
	v_mov_b64_e32 v[4:5], s[18:19]
	v_mad_i64_i32 v[4:5], s[22:23], v16, s80, v[4:5]
	s_waitcnt vmcnt(0)
	v_mul_f32_e32 v16, v15, v56
	v_cvt_pk_bf16_f32 v16, v16, v16
	v_lshlrev_b32_e32 v58, 16, v16
	ds_write_b32 v180, v58 offset:3120
	s_waitcnt vmcnt(0)
	v_mul_f32_e32 v16, v15, v62
	v_cvt_pk_bf16_f32 v16, v16, v16
	s_nop 0
	v_lshlrev_b32_e32 v63, 16, v16
	ds_write_b32 v180, v63 offset:3124
	s_waitcnt vmcnt(0)
	v_mul_f32_e32 v16, v15, v88
	v_cvt_pk_bf16_f32 v16, v16, v16
	v_lshlrev_b32_e32 v91, 16, v16
	v_mov_b32_e32 v16, 0
	ds_write_b32 v180, v91 offset:3128
	s_waitcnt vmcnt(0)
	v_mul_f32_e32 v4, v15, v59
	v_cvt_pk_bf16_f32 v4, v4, v4
	s_and_b64 vcc, exec, s[6:7]
	v_lshlrev_b32_e32 v15, 16, v4
	v_mov_b32_e32 v17, v85
	ds_write_b32 v180, v15 offset:3132
	s_cbranch_vccnz .LBB0_169
	global_load_dword v5, v[0:1], off offset:64
	global_load_dword v4, v[2:3], off offset:64
	s_waitcnt vmcnt(0)
	v_pk_mul_f32 v[16:17], v[84:85], v[4:5] op_sel:[1,0]
.LBB0_169:
	v_or_b32_e32 v18, 16, v86
	v_mov_b64_e32 v[4:5], s[18:19]
	v_mad_i64_i32 v[4:5], s[22:23], v18, s80, v[4:5]
	s_waitcnt vmcnt(0)
	v_mul_f32_e32 v18, v17, v75
	v_cvt_pk_bf16_f32 v18, v18, v18
	s_nop 0
	v_lshlrev_b32_e32 v89, 16, v18
	ds_write_b32 v180, v89 offset:4160
	s_waitcnt vmcnt(0)
	v_mul_f32_e32 v18, v17, v90
	v_cvt_pk_bf16_f32 v18, v18, v18
	v_lshlrev_b32_e32 v93, 16, v18
	ds_write_b32 v180, v93 offset:4164
	s_waitcnt vmcnt(0)
	v_mul_f32_e32 v18, v17, v96
	v_cvt_pk_bf16_f32 v18, v18, v18
	s_nop 0
	v_lshlrev_b32_e32 v97, 16, v18
	ds_write_b32 v180, v97 offset:4168
	s_waitcnt vmcnt(0)
	v_mul_f32_e32 v4, v17, v73
	v_cvt_pk_bf16_f32 v4, v4, v4
	v_lshlrev_b32_e32 v17, 16, v4
	s_and_b64 vcc, exec, s[6:7]
	v_mov_b32_e32 v18, 0
	v_mov_b32_e32 v19, v85
	ds_write_b32 v180, v17 offset:4172
	s_cbranch_vccnz .LBB0_179
	global_load_dword v5, v[0:1], off offset:80
	global_load_dword v4, v[2:3], off offset:80
	s_waitcnt vmcnt(0)
	v_pk_mul_f32 v[18:19], v[84:85], v[4:5] op_sel:[1,0]
.LBB0_179:
	v_or_b32_e32 v20, 20, v86
	v_mov_b64_e32 v[4:5], s[18:19]
	v_mad_i64_i32 v[4:5], s[22:23], v20, s80, v[4:5]
	s_waitcnt vmcnt(0)
	v_mul_f32_e32 v20, v19, v92
	v_cvt_pk_bf16_f32 v20, v20, v20
	v_lshlrev_b32_e32 v94, 16, v20
	ds_write_b32 v180, v94 offset:5200
	s_waitcnt vmcnt(0)
	v_mul_f32_e32 v20, v19, v98
	v_cvt_pk_bf16_f32 v20, v20, v20
	s_nop 0
	v_lshlrev_b32_e32 v99, 16, v20
	ds_write_b32 v180, v99 offset:5204
	s_waitcnt vmcnt(0)
	v_mul_f32_e32 v20, v19, v102
	v_cvt_pk_bf16_f32 v20, v20, v20
	v_lshlrev_b32_e32 v105, 16, v20
	v_mov_b32_e32 v20, 0
	ds_write_b32 v180, v105 offset:5208
	s_waitcnt vmcnt(0)
	v_mul_f32_e32 v4, v19, v95
	v_cvt_pk_bf16_f32 v4, v4, v4
	s_and_b64 vcc, exec, s[6:7]
	v_lshlrev_b32_e32 v19, 16, v4
	v_mov_b32_e32 v21, v85
	ds_write_b32 v180, v19 offset:5212
	s_cbranch_vccnz .LBB0_189
	global_load_dword v5, v[0:1], off offset:96
	global_load_dword v4, v[2:3], off offset:96
	s_waitcnt vmcnt(0)
	v_pk_mul_f32 v[20:21], v[84:85], v[4:5] op_sel:[1,0]
.LBB0_189:
	v_or_b32_e32 v22, 24, v86
	v_mov_b64_e32 v[4:5], s[18:19]
	v_mad_i64_i32 v[4:5], s[22:23], v22, s80, v[4:5]
	s_waitcnt vmcnt(0)
	v_mul_f32_e32 v22, v21, v101
	v_cvt_pk_bf16_f32 v22, v22, v22
	s_nop 0
	v_lshlrev_b32_e32 v103, 16, v22
	ds_write_b32 v180, v103 offset:6240
	s_waitcnt vmcnt(0)
	v_mul_f32_e32 v22, v21, v104
	v_cvt_pk_bf16_f32 v22, v22, v22
	v_lshlrev_b32_e32 v107, 16, v22
	ds_write_b32 v180, v107 offset:6244
	s_waitcnt vmcnt(0)
	v_mul_f32_e32 v22, v21, v110
	v_cvt_pk_bf16_f32 v22, v22, v22
	s_nop 0
	v_lshlrev_b32_e32 v111, 16, v22
	ds_write_b32 v180, v111 offset:6248
	s_waitcnt vmcnt(0)
	v_mul_f32_e32 v4, v21, v100
	v_cvt_pk_bf16_f32 v4, v4, v4
	v_lshlrev_b32_e32 v21, 16, v4
	s_and_b64 vcc, exec, s[6:7]
	v_mov_b32_e32 v22, 0
	v_mov_b32_e32 v23, v85
	ds_write_b32 v180, v21 offset:6252
	s_cbranch_vccnz .LBB0_199
	global_load_dword v5, v[0:1], off offset:112
	global_load_dword v4, v[2:3], off offset:112
	s_waitcnt vmcnt(0)
	v_pk_mul_f32 v[22:23], v[84:85], v[4:5] op_sel:[1,0]
.LBB0_199:
	v_or_b32_e32 v24, 28, v86
	v_mov_b64_e32 v[4:5], s[18:19]
	v_mad_i64_i32 v[4:5], s[22:23], v24, s80, v[4:5]
	s_waitcnt vmcnt(0)
	v_mul_f32_e32 v24, v23, v106
	v_cvt_pk_bf16_f32 v24, v24, v24
	v_lshlrev_b32_e32 v108, 16, v24
	ds_write_b32 v180, v108 offset:7280
	s_waitcnt vmcnt(0)
	v_mul_f32_e32 v24, v23, v112
	v_cvt_pk_bf16_f32 v24, v24, v24
	s_nop 0
	v_lshlrev_b32_e32 v113, 16, v24
	ds_write_b32 v180, v113 offset:7284
	s_waitcnt vmcnt(0)
	v_mul_f32_e32 v24, v23, v116
	v_cvt_pk_bf16_f32 v24, v24, v24
	v_lshlrev_b32_e32 v119, 16, v24
	v_mov_b32_e32 v24, 0
	ds_write_b32 v180, v119 offset:7288
	s_waitcnt vmcnt(0)
	v_mul_f32_e32 v4, v23, v109
	v_cvt_pk_bf16_f32 v4, v4, v4
	s_and_b64 vcc, exec, s[6:7]
	v_lshlrev_b32_e32 v23, 16, v4
	v_mov_b32_e32 v25, v85
	ds_write_b32 v180, v23 offset:7292
	s_cbranch_vccnz .LBB0_209
	global_load_dword v5, v[0:1], off offset:128
	global_load_dword v4, v[2:3], off offset:128
	s_waitcnt vmcnt(0)
	v_pk_mul_f32 v[24:25], v[84:85], v[4:5] op_sel:[1,0]
.LBB0_209:
	v_or_b32_e32 v26, 32, v86
	v_mov_b64_e32 v[4:5], s[18:19]
	v_mad_i64_i32 v[4:5], s[22:23], v26, s80, v[4:5]
	s_waitcnt vmcnt(0)
	v_mul_f32_e32 v26, v25, v115
	v_cvt_pk_bf16_f32 v26, v26, v26
	s_nop 0
	v_lshlrev_b32_e32 v117, 16, v26
	ds_write_b32 v180, v117 offset:8320
	s_waitcnt vmcnt(0)
	v_mul_f32_e32 v26, v25, v118
	v_cvt_pk_bf16_f32 v26, v26, v26
	v_lshlrev_b32_e32 v121, 16, v26
	ds_write_b32 v180, v121 offset:8324
	s_waitcnt vmcnt(0)
	v_mul_f32_e32 v26, v25, v124
	v_cvt_pk_bf16_f32 v26, v26, v26
	s_nop 0
	v_lshlrev_b32_e32 v125, 16, v26
	ds_write_b32 v180, v125 offset:8328
	s_waitcnt vmcnt(0)
	v_mul_f32_e32 v4, v25, v114
	v_cvt_pk_bf16_f32 v4, v4, v4
	v_lshlrev_b32_e32 v25, 16, v4
	s_and_b64 vcc, exec, s[6:7]
	v_mov_b32_e32 v26, 0
	v_mov_b32_e32 v27, v85
	ds_write_b32 v180, v25 offset:8332
	s_cbranch_vccnz .LBB0_219
	global_load_dword v5, v[0:1], off offset:144
	global_load_dword v4, v[2:3], off offset:144
	s_waitcnt vmcnt(0)
	v_pk_mul_f32 v[26:27], v[84:85], v[4:5] op_sel:[1,0]
.LBB0_219:
	v_or_b32_e32 v28, 36, v86
	v_mov_b64_e32 v[4:5], s[18:19]
	v_mad_i64_i32 v[4:5], s[22:23], v28, s80, v[4:5]
	s_waitcnt vmcnt(0)
	v_mul_f32_e32 v28, v27, v120
	v_cvt_pk_bf16_f32 v28, v28, v28
	v_lshlrev_b32_e32 v122, 16, v28
	ds_write_b32 v180, v122 offset:9360
	s_waitcnt vmcnt(0)
	v_mul_f32_e32 v28, v27, v126
	v_cvt_pk_bf16_f32 v28, v28, v28
	s_nop 0
	v_lshlrev_b32_e32 v127, 16, v28
	ds_write_b32 v180, v127 offset:9364
	s_waitcnt vmcnt(0)
	v_mul_f32_e32 v28, v27, v130
	v_cvt_pk_bf16_f32 v28, v28, v28
	v_lshlrev_b32_e32 v133, 16, v28
	v_mov_b32_e32 v28, 0
	ds_write_b32 v180, v133 offset:9368
	s_waitcnt vmcnt(0)
	v_mul_f32_e32 v4, v27, v123
	v_cvt_pk_bf16_f32 v4, v4, v4
	s_and_b64 vcc, exec, s[6:7]
	v_lshlrev_b32_e32 v27, 16, v4
	v_mov_b32_e32 v29, v85
	ds_write_b32 v180, v27 offset:9372
	s_cbranch_vccnz .LBB0_229
	global_load_dword v5, v[0:1], off offset:160
	global_load_dword v4, v[2:3], off offset:160
	s_waitcnt vmcnt(0)
	v_pk_mul_f32 v[28:29], v[84:85], v[4:5] op_sel:[1,0]
.LBB0_229:
	v_or_b32_e32 v30, 40, v86
	v_mov_b64_e32 v[4:5], s[18:19]
	v_mad_i64_i32 v[4:5], s[22:23], v30, s80, v[4:5]
	s_waitcnt vmcnt(0)
	v_mul_f32_e32 v30, v29, v129
	v_cvt_pk_bf16_f32 v30, v30, v30
	s_nop 0
	v_lshlrev_b32_e32 v131, 16, v30
	ds_write_b32 v180, v131 offset:10400
	s_waitcnt vmcnt(0)
	v_mul_f32_e32 v30, v29, v132
	v_cvt_pk_bf16_f32 v30, v30, v30
	v_lshlrev_b32_e32 v135, 16, v30
	ds_write_b32 v180, v135 offset:10404
	s_waitcnt vmcnt(0)
	v_mul_f32_e32 v30, v29, v138
	v_cvt_pk_bf16_f32 v30, v30, v30
	s_nop 0
	v_lshlrev_b32_e32 v139, 16, v30
	ds_write_b32 v180, v139 offset:10408
	s_waitcnt vmcnt(0)
	v_mul_f32_e32 v4, v29, v128
	v_cvt_pk_bf16_f32 v4, v4, v4
	v_lshlrev_b32_e32 v29, 16, v4
	s_and_b64 vcc, exec, s[6:7]
	v_mov_b32_e32 v30, 0
	v_mov_b32_e32 v31, v85
	ds_write_b32 v180, v29 offset:10412
	s_cbranch_vccnz .LBB0_239
	global_load_dword v5, v[0:1], off offset:176
	global_load_dword v4, v[2:3], off offset:176
	s_waitcnt vmcnt(0)
	v_pk_mul_f32 v[30:31], v[84:85], v[4:5] op_sel:[1,0]
.LBB0_239:
	v_or_b32_e32 v32, 44, v86
	v_mov_b64_e32 v[4:5], s[18:19]
	v_mad_i64_i32 v[4:5], s[22:23], v32, s80, v[4:5]
	s_waitcnt vmcnt(0)
	v_mul_f32_e32 v32, v31, v134
	v_cvt_pk_bf16_f32 v32, v32, v32
	v_lshlrev_b32_e32 v136, 16, v32
	ds_write_b32 v180, v136 offset:11440
	s_waitcnt vmcnt(0)
	v_mul_f32_e32 v32, v31, v140
	v_cvt_pk_bf16_f32 v32, v32, v32
	s_nop 0
	v_lshlrev_b32_e32 v141, 16, v32
	ds_write_b32 v180, v141 offset:11444
	s_waitcnt vmcnt(0)
	v_mul_f32_e32 v32, v31, v144
	v_cvt_pk_bf16_f32 v32, v32, v32
	v_lshlrev_b32_e32 v147, 16, v32
	v_mov_b32_e32 v32, 0
	ds_write_b32 v180, v147 offset:11448
	s_waitcnt vmcnt(0)
	v_mul_f32_e32 v4, v31, v137
	v_cvt_pk_bf16_f32 v4, v4, v4
	s_and_b64 vcc, exec, s[6:7]
	v_lshlrev_b32_e32 v31, 16, v4
	v_mov_b32_e32 v33, v85
	ds_write_b32 v180, v31 offset:11452
	s_cbranch_vccnz .LBB0_249
	global_load_dword v5, v[0:1], off offset:192
	global_load_dword v4, v[2:3], off offset:192
	s_waitcnt vmcnt(0)
	v_pk_mul_f32 v[32:33], v[84:85], v[4:5] op_sel:[1,0]
.LBB0_249:
	v_or_b32_e32 v34, 48, v86
	v_mov_b64_e32 v[4:5], s[18:19]
	v_mad_i64_i32 v[4:5], s[22:23], v34, s80, v[4:5]
	s_waitcnt vmcnt(0)
	v_mul_f32_e32 v34, v33, v143
	v_cvt_pk_bf16_f32 v34, v34, v34
	s_nop 0
	v_lshlrev_b32_e32 v145, 16, v34
	ds_write_b32 v180, v145 offset:12480
	s_waitcnt vmcnt(0)
	v_mul_f32_e32 v34, v33, v146
	v_cvt_pk_bf16_f32 v34, v34, v34
	v_lshlrev_b32_e32 v149, 16, v34
	ds_write_b32 v180, v149 offset:12484
	s_waitcnt vmcnt(0)
	v_mul_f32_e32 v34, v33, v152
	v_cvt_pk_bf16_f32 v34, v34, v34
	s_nop 0
	v_lshlrev_b32_e32 v153, 16, v34
	ds_write_b32 v180, v153 offset:12488
	s_waitcnt vmcnt(0)
	v_mul_f32_e32 v4, v33, v142
	v_cvt_pk_bf16_f32 v4, v4, v4
	v_lshlrev_b32_e32 v33, 16, v4
	s_and_b64 vcc, exec, s[6:7]
	v_mov_b32_e32 v34, 0
	v_mov_b32_e32 v35, v85
	ds_write_b32 v180, v33 offset:12492
	s_cbranch_vccnz .LBB0_259
	global_load_dword v5, v[0:1], off offset:208
	global_load_dword v4, v[2:3], off offset:208
	s_waitcnt vmcnt(0)
	v_pk_mul_f32 v[34:35], v[84:85], v[4:5] op_sel:[1,0]
.LBB0_259:
	v_or_b32_e32 v36, 52, v86
	v_mov_b64_e32 v[4:5], s[18:19]
	v_mad_i64_i32 v[4:5], s[22:23], v36, s80, v[4:5]
	s_waitcnt vmcnt(0)
	v_mul_f32_e32 v36, v35, v148
	v_cvt_pk_bf16_f32 v36, v36, v36
	v_lshlrev_b32_e32 v150, 16, v36
	ds_write_b32 v180, v150 offset:13520
	s_waitcnt vmcnt(0)
	v_mul_f32_e32 v36, v35, v154
	v_cvt_pk_bf16_f32 v36, v36, v36
	s_nop 0
	v_lshlrev_b32_e32 v155, 16, v36
	ds_write_b32 v180, v155 offset:13524
	s_waitcnt vmcnt(0)
	v_mul_f32_e32 v36, v35, v158
	v_cvt_pk_bf16_f32 v36, v36, v36
	v_lshlrev_b32_e32 v161, 16, v36
	v_mov_b32_e32 v36, 0
	ds_write_b32 v180, v161 offset:13528
	s_waitcnt vmcnt(0)
	v_mul_f32_e32 v4, v35, v151
	v_cvt_pk_bf16_f32 v4, v4, v4
	s_and_b64 vcc, exec, s[6:7]
	v_lshlrev_b32_e32 v35, 16, v4
	v_mov_b32_e32 v37, v85
	ds_write_b32 v180, v35 offset:13532
	s_cbranch_vccnz .LBB0_269
	global_load_dword v5, v[0:1], off offset:224
	global_load_dword v4, v[2:3], off offset:224
	s_waitcnt vmcnt(0)
	v_pk_mul_f32 v[36:37], v[84:85], v[4:5] op_sel:[1,0]
.LBB0_269:
	v_or_b32_e32 v38, 56, v86
	v_mov_b64_e32 v[4:5], s[18:19]
	v_mad_i64_i32 v[4:5], s[22:23], v38, s80, v[4:5]
	s_waitcnt vmcnt(0)
	v_mul_f32_e32 v38, v37, v157
	v_cvt_pk_bf16_f32 v38, v38, v38
	s_nop 0
	v_lshlrev_b32_e32 v159, 16, v38
	ds_write_b32 v180, v159 offset:14560
	s_waitcnt vmcnt(0)
	v_mul_f32_e32 v38, v37, v160
	v_cvt_pk_bf16_f32 v38, v38, v38
	v_lshlrev_b32_e32 v163, 16, v38
	ds_write_b32 v180, v163 offset:14564
	s_waitcnt vmcnt(0)
	v_mul_f32_e32 v38, v37, v164
	v_cvt_pk_bf16_f32 v38, v38, v38
	s_nop 0
	v_lshlrev_b32_e32 v165, 16, v38
	ds_write_b32 v180, v165 offset:14568
	s_waitcnt vmcnt(0)
	v_mul_f32_e32 v4, v37, v156
	v_cvt_pk_bf16_f32 v4, v4, v4
	v_mov_b32_e32 v162, 0
	v_lshlrev_b32_e32 v37, 16, v4
	s_and_b64 vcc, exec, s[6:7]
	v_mov_b32_e32 v38, 0
	v_mov_b32_e32 v39, v85
	ds_write_b32 v180, v37 offset:14572
	s_cbranch_vccnz .LBB0_279
	global_load_dword v1, v[0:1], off offset:240
	s_nop 0
	global_load_dword v0, v[2:3], off offset:240
	s_waitcnt vmcnt(0)
	v_pk_mul_f32 v[38:39], v[84:85], v[0:1] op_sel:[1,0]

.LBB0_1134:
	s_cmp_eq_u32 s42, -2
	s_cselect_b64 s[10:11], -1, 0
	v_mov_b64_e32 v[8:9], s[50:51]
	v_mad_i64_i32 v[8:9], s[40:41], v2, s94, v[8:9]
	s_and_b64 s[52:53], s[10:11], s[38:39]
	v_mov_b32_e32 v45, 0
	v_mov_b32_e32 v43, 0
	s_waitcnt vmcnt(0)
	v_mov_b32_e32 v43, 0
	v_mov_b32_e32 v45, 0
	v_mov_b32_e32 v50, 0
	v_mov_b32_e32 v42, 0
	v_mov_b32_e32 v46, 0
	v_mov_b32_e32 v52, 0
	v_mov_b32_e32 v56, 0
	v_mov_b32_e32 v49, 0
	v_mov_b32_e32 v55, 0
	v_mov_b32_e32 v58, 0
	v_mov_b32_e32 v64, 0
	v_mov_b32_e32 v54, 0
	v_mov_b32_e32 v60, 0
	v_mov_b32_e32 v110, 0
	v_mov_b32_e32 v114, 0
	v_mov_b32_e32 v63, 0
	v_mov_b32_e32 v113, 0
	v_mov_b32_e32 v116, 0
	v_mov_b32_e32 v122, 0
	v_mov_b32_e32 v112, 0
	v_mov_b32_e32 v118, 0
	v_mov_b32_e32 v124, 0
	v_mov_b32_e32 v128, 0
	v_mov_b32_e32 v121, 0
	v_mov_b32_e32 v127, 0
	v_mov_b32_e32 v130, 0
	v_mov_b32_e32 v136, 0
	v_mov_b32_e32 v126, 0
	v_mov_b32_e32 v132, 0
	v_mov_b32_e32 v138, 0
	v_mov_b32_e32 v142, 0
	v_mov_b32_e32 v135, 0
	v_mov_b32_e32 v141, 0
	v_mov_b32_e32 v144, 0
	v_mov_b32_e32 v150, 0
	v_mov_b32_e32 v140, 0
	v_mov_b32_e32 v146, 0
	v_mov_b32_e32 v152, 0
	v_mov_b32_e32 v156, 0
	v_mov_b32_e32 v149, 0
	v_mov_b32_e32 v155, 0
	v_mov_b32_e32 v158, 0
	v_mov_b32_e32 v164, 0
	v_mov_b32_e32 v154, 0
	v_mov_b32_e32 v160, 0
	v_mov_b32_e32 v166, 0
	v_mov_b32_e32 v170, 0
	v_mov_b32_e32 v163, 0
	v_mov_b32_e32 v169, 0
	v_mov_b32_e32 v172, 0
	v_mov_b32_e32 v178, 0
	v_mov_b32_e32 v168, 0
	v_mov_b32_e32 v174, 0
	v_mov_b32_e32 v180, 0
	v_mov_b32_e32 v184, 0
	v_mov_b32_e32 v177, 0
	v_mov_b32_e32 v183, 0
	v_mov_b32_e32 v186, 0
	v_mov_b32_e32 v190, 0
	v_mov_b32_e32 v182, 0
	s_and_saveexec_b64 s[40:41], s[52:53]
	s_cbranch_execz .Lgate_batch_done_mix
	v_mov_b32_e32 v12, 0x4d180
	v_mov_b32_e32 v13, 0
	v_lshlrev_b32_e32 v0, 2, v74
	v_lshl_add_u64 v[8:9], v[8:9], 0, v[0:1]
	global_load_dword v43, v[8:9], off
	global_load_dword v45, v[8:9], off offset:4
	global_load_dword v50, v[8:9], off offset:8
	global_load_dword v42, v[8:9], off offset:12
	v_lshl_add_u64 v[8:9], v[8:9], 0, v[12:13]
	global_load_dword v46, v[8:9], off
	global_load_dword v52, v[8:9], off offset:4
	global_load_dword v56, v[8:9], off offset:8
	global_load_dword v49, v[8:9], off offset:12
	v_lshl_add_u64 v[8:9], v[8:9], 0, v[12:13]
	global_load_dword v55, v[8:9], off
	global_load_dword v58, v[8:9], off offset:4
	global_load_dword v64, v[8:9], off offset:8
	global_load_dword v54, v[8:9], off offset:12
	v_lshl_add_u64 v[8:9], v[8:9], 0, v[12:13]
	global_load_dword v60, v[8:9], off
	global_load_dword v110, v[8:9], off offset:4
	global_load_dword v114, v[8:9], off offset:8
	global_load_dword v63, v[8:9], off offset:12
	v_lshl_add_u64 v[8:9], v[8:9], 0, v[12:13]
	global_load_dword v113, v[8:9], off
	global_load_dword v116, v[8:9], off offset:4
	global_load_dword v122, v[8:9], off offset:8
	global_load_dword v112, v[8:9], off offset:12
	v_lshl_add_u64 v[8:9], v[8:9], 0, v[12:13]
	global_load_dword v118, v[8:9], off
	global_load_dword v124, v[8:9], off offset:4
	global_load_dword v128, v[8:9], off offset:8
	global_load_dword v121, v[8:9], off offset:12
	v_lshl_add_u64 v[8:9], v[8:9], 0, v[12:13]
	global_load_dword v127, v[8:9], off
	global_load_dword v130, v[8:9], off offset:4
	global_load_dword v136, v[8:9], off offset:8
	global_load_dword v126, v[8:9], off offset:12
	v_lshl_add_u64 v[8:9], v[8:9], 0, v[12:13]
	global_load_dword v132, v[8:9], off
	global_load_dword v138, v[8:9], off offset:4
	global_load_dword v142, v[8:9], off offset:8
	global_load_dword v135, v[8:9], off offset:12
	v_lshl_add_u64 v[8:9], v[8:9], 0, v[12:13]
	global_load_dword v141, v[8:9], off
	global_load_dword v144, v[8:9], off offset:4
	global_load_dword v150, v[8:9], off offset:8
	global_load_dword v140, v[8:9], off offset:12
	v_lshl_add_u64 v[8:9], v[8:9], 0, v[12:13]
	global_load_dword v146, v[8:9], off
	global_load_dword v152, v[8:9], off offset:4
	global_load_dword v156, v[8:9], off offset:8
	global_load_dword v149, v[8:9], off offset:12
	v_lshl_add_u64 v[8:9], v[8:9], 0, v[12:13]
	global_load_dword v155, v[8:9], off
	global_load_dword v158, v[8:9], off offset:4
	global_load_dword v164, v[8:9], off offset:8
	global_load_dword v154, v[8:9], off offset:12
	v_lshl_add_u64 v[8:9], v[8:9], 0, v[12:13]
	global_load_dword v160, v[8:9], off
	global_load_dword v166, v[8:9], off offset:4
	global_load_dword v170, v[8:9], off offset:8
	global_load_dword v163, v[8:9], off offset:12
	v_lshl_add_u64 v[8:9], v[8:9], 0, v[12:13]
	global_load_dword v169, v[8:9], off
	global_load_dword v172, v[8:9], off offset:4
	global_load_dword v178, v[8:9], off offset:8
	global_load_dword v168, v[8:9], off offset:12
	v_lshl_add_u64 v[8:9], v[8:9], 0, v[12:13]
	global_load_dword v174, v[8:9], off
	global_load_dword v180, v[8:9], off offset:4
	global_load_dword v184, v[8:9], off offset:8
	global_load_dword v177, v[8:9], off offset:12
	v_lshl_add_u64 v[8:9], v[8:9], 0, v[12:13]
	global_load_dword v183, v[8:9], off
	global_load_dword v186, v[8:9], off offset:4
	global_load_dword v190, v[8:9], off offset:8
	global_load_dword v182, v[8:9], off offset:12
.Lgate_batch_done_mix:
	s_or_b64 exec, exec, s[40:41]
	s_waitcnt vmcnt(0)
	v_mul_f32_e32 v0, v7, v43
	v_cvt_pk_bf16_f32 v0, v0, v0
	s_nop 0
	v_lshlrev_b32_e32 v44, 16, v0
	ds_write_b32 v69, v44
	s_waitcnt vmcnt(0)
	v_mul_f32_e32 v0, v7, v45
	v_cvt_pk_bf16_f32 v0, v0, v0
	v_lshlrev_b32_e32 v47, 16, v0
	ds_write_b32 v69, v47 offset:4
	s_waitcnt vmcnt(0)
	v_mul_f32_e32 v0, v7, v50
	v_cvt_pk_bf16_f32 v0, v0, v0
	s_nop 0
	v_lshlrev_b32_e32 v51, 16, v0
	ds_write_b32 v69, v51 offset:8
	s_waitcnt vmcnt(0)
	v_mul_f32_e32 v0, v7, v42
	v_cvt_pk_bf16_f32 v0, v0, v0
	v_lshlrev_b32_e32 v7, 16, v0
	v_cndmask_b32_e64 v0, 0, 1, s[54:55]
	v_cmp_ne_u32_e64 s[40:41], 1, v0
	s_andn2_b64 vcc, exec, s[54:55]
	v_mov_b32_e32 v8, 0
	v_mov_b32_e32 v9, v109
	ds_write_b32 v69, v7 offset:12
	s_cbranch_vccnz .LBB0_1144
	global_load_dword v9, v[4:5], off offset:16
	global_load_dword v8, v[10:11], off offset:16
	s_waitcnt vmcnt(0)
	v_pk_mul_f32 v[8:9], v[108:109], v[8:9] op_sel:[1,0]
.LBB0_1144:
	v_add_u32_e32 v0, 4, v2
	v_mov_b64_e32 v[12:13], s[50:51]
	v_mad_i64_i32 v[14:15], s[10:11], v0, s94, v[12:13]
	s_waitcnt vmcnt(0)
	v_mul_f32_e32 v0, v9, v46
	v_cvt_pk_bf16_f32 v0, v0, v0
	v_lshlrev_b32_e32 v48, 16, v0
	ds_write_b32 v69, v48 offset:1040
	s_waitcnt vmcnt(0)
	v_mul_f32_e32 v0, v9, v52
	v_cvt_pk_bf16_f32 v0, v0, v0
	s_nop 0
	v_lshlrev_b32_e32 v53, 16, v0
	ds_write_b32 v69, v53 offset:1044
	s_waitcnt vmcnt(0)
	v_mul_f32_e32 v0, v9, v56
	v_cvt_pk_bf16_f32 v0, v0, v0
	v_mov_b32_e32 v12, 0
	v_lshlrev_b32_e32 v59, 16, v0
	ds_write_b32 v69, v59 offset:1048
	s_waitcnt vmcnt(0)
	v_mul_f32_e32 v0, v9, v49
	v_cvt_pk_bf16_f32 v0, v0, v0
	s_and_b64 vcc, exec, s[40:41]
	v_lshlrev_b32_e32 v9, 16, v0
	v_mov_b32_e32 v13, v109
	ds_write_b32 v69, v9 offset:1052
	s_cbranch_vccnz .LBB0_1154
	global_load_dword v13, v[4:5], off offset:32
	global_load_dword v12, v[10:11], off offset:32
	s_waitcnt vmcnt(0)
	v_pk_mul_f32 v[12:13], v[108:109], v[12:13] op_sel:[1,0]
.LBB0_1154:
	v_add_u32_e32 v0, 8, v2
	v_mov_b64_e32 v[14:15], s[50:51]
	v_mad_i64_i32 v[14:15], s[10:11], v0, s94, v[14:15]
	s_waitcnt vmcnt(0)
	v_mul_f32_e32 v0, v13, v55
	v_cvt_pk_bf16_f32 v0, v0, v0
	s_nop 0
	v_lshlrev_b32_e32 v57, 16, v0
	ds_write_b32 v69, v57 offset:2080
	s_waitcnt vmcnt(0)
	v_mul_f32_e32 v0, v13, v58
	v_cvt_pk_bf16_f32 v0, v0, v0
	v_lshlrev_b32_e32 v61, 16, v0
	ds_write_b32 v69, v61 offset:2084
	s_waitcnt vmcnt(0)
	v_mul_f32_e32 v0, v13, v64
	v_cvt_pk_bf16_f32 v0, v0, v0
	s_nop 0
	v_lshlrev_b32_e32 v65, 16, v0
	ds_write_b32 v69, v65 offset:2088
	s_waitcnt vmcnt(0)
	v_mul_f32_e32 v0, v13, v54
	v_cvt_pk_bf16_f32 v0, v0, v0
	v_lshlrev_b32_e32 v13, 16, v0
	s_and_b64 vcc, exec, s[40:41]
	v_mov_b32_e32 v14, 0
	v_mov_b32_e32 v15, v109
	ds_write_b32 v69, v13 offset:2092
	s_cbranch_vccnz .LBB0_1164
	global_load_dword v15, v[4:5], off offset:48
	global_load_dword v14, v[10:11], off offset:48
	s_waitcnt vmcnt(0)
	v_pk_mul_f32 v[14:15], v[108:109], v[14:15] op_sel:[1,0]
.LBB0_1164:
	v_add_u32_e32 v0, 12, v2
	v_mov_b64_e32 v[16:17], s[50:51]
	v_mad_i64_i32 v[18:19], s[10:11], v0, s94, v[16:17]
	s_waitcnt vmcnt(0)
	v_mul_f32_e32 v0, v15, v60
	v_cvt_pk_bf16_f32 v0, v0, v0
	v_lshlrev_b32_e32 v62, 16, v0
	ds_write_b32 v69, v62 offset:3120
	s_waitcnt vmcnt(0)
	v_mul_f32_e32 v0, v15, v110
	v_cvt_pk_bf16_f32 v0, v0, v0
	s_nop 0
	v_lshlrev_b32_e32 v111, 16, v0
	ds_write_b32 v69, v111 offset:3124
	s_waitcnt vmcnt(0)
	v_mul_f32_e32 v0, v15, v114
	v_cvt_pk_bf16_f32 v0, v0, v0
	v_mov_b32_e32 v16, 0
	v_lshlrev_b32_e32 v117, 16, v0
	ds_write_b32 v69, v117 offset:3128
	s_waitcnt vmcnt(0)
	v_mul_f32_e32 v0, v15, v63
	v_cvt_pk_bf16_f32 v0, v0, v0
	s_and_b64 vcc, exec, s[40:41]
	v_lshlrev_b32_e32 v15, 16, v0
	v_mov_b32_e32 v17, v109
	ds_write_b32 v69, v15 offset:3132
	s_cbranch_vccnz .LBB0_1174
	global_load_dword v17, v[4:5], off offset:64
	global_load_dword v16, v[10:11], off offset:64
	s_waitcnt vmcnt(0)
	v_pk_mul_f32 v[16:17], v[108:109], v[16:17] op_sel:[1,0]
.LBB0_1174:
	v_add_u32_e32 v0, 16, v2
	v_mov_b64_e32 v[18:19], s[50:51]
	v_mad_i64_i32 v[18:19], s[10:11], v0, s94, v[18:19]
	s_waitcnt vmcnt(0)
	v_mul_f32_e32 v0, v17, v113
	v_cvt_pk_bf16_f32 v0, v0, v0
	s_nop 0
	v_lshlrev_b32_e32 v115, 16, v0
	ds_write_b32 v69, v115 offset:4160
	s_waitcnt vmcnt(0)
	v_mul_f32_e32 v0, v17, v116
	v_cvt_pk_bf16_f32 v0, v0, v0
	v_lshlrev_b32_e32 v119, 16, v0
	ds_write_b32 v69, v119 offset:4164
	s_waitcnt vmcnt(0)
	v_mul_f32_e32 v0, v17, v122
	v_cvt_pk_bf16_f32 v0, v0, v0
	s_nop 0
	v_lshlrev_b32_e32 v123, 16, v0
	ds_write_b32 v69, v123 offset:4168
	s_waitcnt vmcnt(0)
	v_mul_f32_e32 v0, v17, v112
	v_cvt_pk_bf16_f32 v0, v0, v0
	v_lshlrev_b32_e32 v17, 16, v0
	s_and_b64 vcc, exec, s[40:41]
	v_mov_b32_e32 v18, 0
	v_mov_b32_e32 v19, v109
	ds_write_b32 v69, v17 offset:4172
	s_cbranch_vccnz .LBB0_1184
	global_load_dword v19, v[4:5], off offset:80
	global_load_dword v18, v[10:11], off offset:80
	s_waitcnt vmcnt(0)
	v_pk_mul_f32 v[18:19], v[108:109], v[18:19] op_sel:[1,0]
.LBB0_1184:
	v_add_u32_e32 v0, 20, v2
	v_mov_b64_e32 v[20:21], s[50:51]
	v_mad_i64_i32 v[22:23], s[10:11], v0, s94, v[20:21]
	s_waitcnt vmcnt(0)
	v_mul_f32_e32 v0, v19, v118
	v_cvt_pk_bf16_f32 v0, v0, v0
	v_lshlrev_b32_e32 v120, 16, v0
	ds_write_b32 v69, v120 offset:5200
	s_waitcnt vmcnt(0)
	v_mul_f32_e32 v0, v19, v124
	v_cvt_pk_bf16_f32 v0, v0, v0
	s_nop 0
	v_lshlrev_b32_e32 v125, 16, v0
	ds_write_b32 v69, v125 offset:5204
	s_waitcnt vmcnt(0)
	v_mul_f32_e32 v0, v19, v128
	v_cvt_pk_bf16_f32 v0, v0, v0
	v_mov_b32_e32 v20, 0
	v_lshlrev_b32_e32 v131, 16, v0
	ds_write_b32 v69, v131 offset:5208
	s_waitcnt vmcnt(0)
	v_mul_f32_e32 v0, v19, v121
	v_cvt_pk_bf16_f32 v0, v0, v0
	s_and_b64 vcc, exec, s[40:41]
	v_lshlrev_b32_e32 v19, 16, v0
	v_mov_b32_e32 v21, v109
	ds_write_b32 v69, v19 offset:5212
	s_cbranch_vccnz .LBB0_1194
	global_load_dword v21, v[4:5], off offset:96
	global_load_dword v20, v[10:11], off offset:96
	s_waitcnt vmcnt(0)
	v_pk_mul_f32 v[20:21], v[108:109], v[20:21] op_sel:[1,0]
.LBB0_1194:
	v_add_u32_e32 v0, 24, v2
	v_mov_b64_e32 v[22:23], s[50:51]
	v_mad_i64_i32 v[22:23], s[10:11], v0, s94, v[22:23]
	s_waitcnt vmcnt(0)
	v_mul_f32_e32 v0, v21, v127
	v_cvt_pk_bf16_f32 v0, v0, v0
	s_nop 0
	v_lshlrev_b32_e32 v129, 16, v0
	ds_write_b32 v69, v129 offset:6240
	s_waitcnt vmcnt(0)
	v_mul_f32_e32 v0, v21, v130
	v_cvt_pk_bf16_f32 v0, v0, v0
	v_lshlrev_b32_e32 v133, 16, v0
	ds_write_b32 v69, v133 offset:6244
	s_waitcnt vmcnt(0)
	v_mul_f32_e32 v0, v21, v136
	v_cvt_pk_bf16_f32 v0, v0, v0
	s_nop 0
	v_lshlrev_b32_e32 v137, 16, v0
	ds_write_b32 v69, v137 offset:6248
	s_waitcnt vmcnt(0)
	v_mul_f32_e32 v0, v21, v126
	v_cvt_pk_bf16_f32 v0, v0, v0
	v_lshlrev_b32_e32 v21, 16, v0
	s_and_b64 vcc, exec, s[40:41]
	v_mov_b32_e32 v22, 0
	v_mov_b32_e32 v23, v109
	ds_write_b32 v69, v21 offset:6252
	s_cbranch_vccnz .LBB0_1204
	global_load_dword v23, v[4:5], off offset:112
	global_load_dword v22, v[10:11], off offset:112
	s_waitcnt vmcnt(0)
	v_pk_mul_f32 v[22:23], v[108:109], v[22:23] op_sel:[1,0]
.LBB0_1204:
	v_add_u32_e32 v0, 28, v2
	v_mov_b64_e32 v[24:25], s[50:51]
	v_mad_i64_i32 v[26:27], s[10:11], v0, s94, v[24:25]
	s_waitcnt vmcnt(0)
	v_mul_f32_e32 v0, v23, v132
	v_cvt_pk_bf16_f32 v0, v0, v0
	v_lshlrev_b32_e32 v134, 16, v0
	ds_write_b32 v69, v134 offset:7280
	s_waitcnt vmcnt(0)
	v_mul_f32_e32 v0, v23, v138
	v_cvt_pk_bf16_f32 v0, v0, v0
	s_nop 0
	v_lshlrev_b32_e32 v139, 16, v0
	ds_write_b32 v69, v139 offset:7284
	s_waitcnt vmcnt(0)
	v_mul_f32_e32 v0, v23, v142
	v_cvt_pk_bf16_f32 v0, v0, v0
	v_mov_b32_e32 v24, 0
	v_lshlrev_b32_e32 v145, 16, v0
	ds_write_b32 v69, v145 offset:7288
	s_waitcnt vmcnt(0)
	v_mul_f32_e32 v0, v23, v135
	v_cvt_pk_bf16_f32 v0, v0, v0
	s_and_b64 vcc, exec, s[40:41]
	v_lshlrev_b32_e32 v23, 16, v0
	v_mov_b32_e32 v25, v109
	ds_write_b32 v69, v23 offset:7292
	s_cbranch_vccnz .LBB0_1214
	global_load_dword v25, v[4:5], off offset:128
	global_load_dword v24, v[10:11], off offset:128
	s_waitcnt vmcnt(0)
	v_pk_mul_f32 v[24:25], v[108:109], v[24:25] op_sel:[1,0]
.LBB0_1214:
	v_add_u32_e32 v0, 32, v2
	v_mov_b64_e32 v[26:27], s[50:51]
	v_mad_i64_i32 v[26:27], s[10:11], v0, s94, v[26:27]
	s_waitcnt vmcnt(0)
	v_mul_f32_e32 v0, v25, v141
	v_cvt_pk_bf16_f32 v0, v0, v0
	s_nop 0
	v_lshlrev_b32_e32 v143, 16, v0
	ds_write_b32 v69, v143 offset:8320
	s_waitcnt vmcnt(0)
	v_mul_f32_e32 v0, v25, v144
	v_cvt_pk_bf16_f32 v0, v0, v0
	v_lshlrev_b32_e32 v147, 16, v0
	ds_write_b32 v69, v147 offset:8324
	s_waitcnt vmcnt(0)
	v_mul_f32_e32 v0, v25, v150
	v_cvt_pk_bf16_f32 v0, v0, v0
	s_nop 0
	v_lshlrev_b32_e32 v151, 16, v0
	ds_write_b32 v69, v151 offset:8328
	s_waitcnt vmcnt(0)
	v_mul_f32_e32 v0, v25, v140
	v_cvt_pk_bf16_f32 v0, v0, v0
	v_lshlrev_b32_e32 v25, 16, v0
	s_and_b64 vcc, exec, s[40:41]
	v_mov_b32_e32 v26, 0
	v_mov_b32_e32 v27, v109
	ds_write_b32 v69, v25 offset:8332
	s_cbranch_vccnz .LBB0_1224
	global_load_dword v27, v[4:5], off offset:144
	global_load_dword v26, v[10:11], off offset:144
	s_waitcnt vmcnt(0)
	v_pk_mul_f32 v[26:27], v[108:109], v[26:27] op_sel:[1,0]
.LBB0_1224:
	v_add_u32_e32 v0, 36, v2
	v_mov_b64_e32 v[28:29], s[50:51]
	v_mad_i64_i32 v[30:31], s[10:11], v0, s94, v[28:29]
	s_waitcnt vmcnt(0)
	v_mul_f32_e32 v0, v27, v146
	v_cvt_pk_bf16_f32 v0, v0, v0
	v_lshlrev_b32_e32 v148, 16, v0
	ds_write_b32 v69, v148 offset:9360
	s_waitcnt vmcnt(0)
	v_mul_f32_e32 v0, v27, v152
	v_cvt_pk_bf16_f32 v0, v0, v0
	s_nop 0
	v_lshlrev_b32_e32 v153, 16, v0
	ds_write_b32 v69, v153 offset:9364
	s_waitcnt vmcnt(0)
	v_mul_f32_e32 v0, v27, v156
	v_cvt_pk_bf16_f32 v0, v0, v0
	v_mov_b32_e32 v28, 0
	v_lshlrev_b32_e32 v159, 16, v0
	ds_write_b32 v69, v159 offset:9368
	s_waitcnt vmcnt(0)
	v_mul_f32_e32 v0, v27, v149
	v_cvt_pk_bf16_f32 v0, v0, v0
	s_and_b64 vcc, exec, s[40:41]
	v_lshlrev_b32_e32 v27, 16, v0
	v_mov_b32_e32 v29, v109
	ds_write_b32 v69, v27 offset:9372
	s_cbranch_vccnz .LBB0_1234
	global_load_dword v29, v[4:5], off offset:160
	global_load_dword v28, v[10:11], off offset:160
	s_waitcnt vmcnt(0)
	v_pk_mul_f32 v[28:29], v[108:109], v[28:29] op_sel:[1,0]
.LBB0_1234:
	v_add_u32_e32 v0, 40, v2
	v_mov_b64_e32 v[30:31], s[50:51]
	v_mad_i64_i32 v[30:31], s[10:11], v0, s94, v[30:31]
	s_waitcnt vmcnt(0)
	v_mul_f32_e32 v0, v29, v155
	v_cvt_pk_bf16_f32 v0, v0, v0
	s_nop 0
	v_lshlrev_b32_e32 v157, 16, v0
	ds_write_b32 v69, v157 offset:10400
	s_waitcnt vmcnt(0)
	v_mul_f32_e32 v0, v29, v158
	v_cvt_pk_bf16_f32 v0, v0, v0
	v_lshlrev_b32_e32 v161, 16, v0
	ds_write_b32 v69, v161 offset:10404
	s_waitcnt vmcnt(0)
	v_mul_f32_e32 v0, v29, v164
	v_cvt_pk_bf16_f32 v0, v0, v0
	s_nop 0
	v_lshlrev_b32_e32 v165, 16, v0
	ds_write_b32 v69, v165 offset:10408
	s_waitcnt vmcnt(0)
	v_mul_f32_e32 v0, v29, v154
	v_cvt_pk_bf16_f32 v0, v0, v0
	v_lshlrev_b32_e32 v29, 16, v0
	s_and_b64 vcc, exec, s[40:41]
	v_mov_b32_e32 v30, 0
	v_mov_b32_e32 v31, v109
	ds_write_b32 v69, v29 offset:10412
	s_cbranch_vccnz .LBB0_1244
	global_load_dword v31, v[4:5], off offset:176
	global_load_dword v30, v[10:11], off offset:176
	s_waitcnt vmcnt(0)
	v_pk_mul_f32 v[30:31], v[108:109], v[30:31] op_sel:[1,0]
.LBB0_1244:
	v_add_u32_e32 v0, 44, v2
	v_mov_b64_e32 v[32:33], s[50:51]
	v_mad_i64_i32 v[34:35], s[10:11], v0, s94, v[32:33]
	s_waitcnt vmcnt(0)
	v_mul_f32_e32 v0, v31, v160
	v_cvt_pk_bf16_f32 v0, v0, v0
	v_lshlrev_b32_e32 v162, 16, v0
	ds_write_b32 v69, v162 offset:11440
	s_waitcnt vmcnt(0)
	v_mul_f32_e32 v0, v31, v166
	v_cvt_pk_bf16_f32 v0, v0, v0
	s_nop 0
	v_lshlrev_b32_e32 v167, 16, v0
	ds_write_b32 v69, v167 offset:11444
	s_waitcnt vmcnt(0)
	v_mul_f32_e32 v0, v31, v170
	v_cvt_pk_bf16_f32 v0, v0, v0
	v_mov_b32_e32 v32, 0
	v_lshlrev_b32_e32 v173, 16, v0
	ds_write_b32 v69, v173 offset:11448
	s_waitcnt vmcnt(0)
	v_mul_f32_e32 v0, v31, v163
	v_cvt_pk_bf16_f32 v0, v0, v0
	s_and_b64 vcc, exec, s[40:41]
	v_lshlrev_b32_e32 v31, 16, v0
	v_mov_b32_e32 v33, v109
	ds_write_b32 v69, v31 offset:11452
	s_cbranch_vccnz .LBB0_1254
	global_load_dword v33, v[4:5], off offset:192
	global_load_dword v32, v[10:11], off offset:192
	s_waitcnt vmcnt(0)
	v_pk_mul_f32 v[32:33], v[108:109], v[32:33] op_sel:[1,0]
.LBB0_1254:
	v_add_u32_e32 v0, 48, v2
	v_mov_b64_e32 v[34:35], s[50:51]
	v_mad_i64_i32 v[34:35], s[10:11], v0, s94, v[34:35]
	s_waitcnt vmcnt(0)
	v_mul_f32_e32 v0, v33, v169
	v_cvt_pk_bf16_f32 v0, v0, v0
	s_nop 0
	v_lshlrev_b32_e32 v171, 16, v0
	ds_write_b32 v69, v171 offset:12480
	s_waitcnt vmcnt(0)
	v_mul_f32_e32 v0, v33, v172
	v_cvt_pk_bf16_f32 v0, v0, v0
	v_lshlrev_b32_e32 v175, 16, v0
	ds_write_b32 v69, v175 offset:12484
	s_waitcnt vmcnt(0)
	v_mul_f32_e32 v0, v33, v178
	v_cvt_pk_bf16_f32 v0, v0, v0
	s_nop 0
	v_lshlrev_b32_e32 v179, 16, v0
	ds_write_b32 v69, v179 offset:12488
	s_waitcnt vmcnt(0)
	v_mul_f32_e32 v0, v33, v168
	v_cvt_pk_bf16_f32 v0, v0, v0
	v_lshlrev_b32_e32 v33, 16, v0
	s_and_b64 vcc, exec, s[40:41]
	v_mov_b32_e32 v36, 0
	v_mov_b32_e32 v37, v109
	ds_write_b32 v69, v33 offset:12492
	s_cbranch_vccnz .LBB0_1264
	global_load_dword v35, v[4:5], off offset:208
	global_load_dword v34, v[10:11], off offset:208
	s_waitcnt vmcnt(0)
	v_pk_mul_f32 v[36:37], v[108:109], v[34:35] op_sel:[1,0]
.LBB0_1264:
	v_add_u32_e32 v0, 52, v2
	v_mov_b64_e32 v[34:35], s[50:51]
	v_mad_i64_i32 v[34:35], s[10:11], v0, s94, v[34:35]
	s_waitcnt vmcnt(0)
	v_mul_f32_e32 v0, v37, v174
	v_cvt_pk_bf16_f32 v0, v0, v0
	v_lshlrev_b32_e32 v176, 16, v0
	ds_write_b32 v69, v176 offset:13520
	s_waitcnt vmcnt(0)
	v_mul_f32_e32 v0, v37, v180
	v_cvt_pk_bf16_f32 v0, v0, v0
	s_nop 0
	v_lshlrev_b32_e32 v181, 16, v0
	ds_write_b32 v69, v181 offset:13524
	s_waitcnt vmcnt(0)
	v_mul_f32_e32 v0, v37, v184
	v_cvt_pk_bf16_f32 v0, v0, v0
	v_mov_b32_e32 v38, 0
	v_lshlrev_b32_e32 v187, 16, v0
	ds_write_b32 v69, v187 offset:13528
	s_waitcnt vmcnt(0)
	v_mul_f32_e32 v0, v37, v177
	v_cvt_pk_bf16_f32 v0, v0, v0
	s_and_b64 vcc, exec, s[40:41]
	v_lshlrev_b32_e32 v37, 16, v0
	v_mov_b32_e32 v39, v109
	ds_write_b32 v69, v37 offset:13532
	s_cbranch_vccnz .LBB0_1274
	global_load_dword v35, v[4:5], off offset:224
	global_load_dword v34, v[10:11], off offset:224
	s_waitcnt vmcnt(0)
	v_pk_mul_f32 v[38:39], v[108:109], v[34:35] op_sel:[1,0]
.LBB0_1274:
	v_add_u32_e32 v0, 56, v2
	v_mov_b64_e32 v[34:35], s[50:51]
	v_mad_i64_i32 v[34:35], s[10:11], v0, s94, v[34:35]
	s_waitcnt vmcnt(0)
	v_mul_f32_e32 v0, v39, v183
	v_cvt_pk_bf16_f32 v0, v0, v0
	s_nop 0
	v_lshlrev_b32_e32 v185, 16, v0
	ds_write_b32 v69, v185 offset:14560
	s_waitcnt vmcnt(0)
	v_mul_f32_e32 v0, v39, v186
	v_cvt_pk_bf16_f32 v0, v0, v0
	v_lshlrev_b32_e32 v189, 16, v0
	ds_write_b32 v69, v189 offset:14564
	s_waitcnt vmcnt(0)
	v_mul_f32_e32 v0, v39, v190
	v_cvt_pk_bf16_f32 v0, v0, v0
	s_nop 0
	v_lshlrev_b32_e32 v191, 16, v0
	ds_write_b32 v69, v191 offset:14568
	s_waitcnt vmcnt(0)
	v_mul_f32_e32 v0, v39, v182
	v_cvt_pk_bf16_f32 v0, v0, v0
	v_mov_b32_e32 v188, 0
	v_lshlrev_b32_e32 v39, 16, v0
	s_and_b64 vcc, exec, s[40:41]
	v_mov_b32_e32 v40, 0
	v_mov_b32_e32 v41, v109
	ds_write_b32 v69, v39 offset:14572
	s_cbranch_vccnz .LBB0_1284
	global_load_dword v5, v[4:5], off offset:240
	s_nop 0
	global_load_dword v4, v[10:11], off offset:240
	s_waitcnt vmcnt(0)
	v_pk_mul_f32 v[40:41], v[108:109], v[4:5] op_sel:[1,0]
